# P3 item prologue: the 20 forget-gate / norm-partial loads of the five serial rounds are touched together up front so the serial rounds hit in cache
# baseline (speedup 1.0000x reference)
; __device__ __forceinline__ int pg8_lane_id() { int l; asm volatile("v_mbcnt_lo_u32_b32 %0, -1, 0\n\tv_mbcnt_hi_u32_b32 %0, -1, %0" : "=v"(l)); return l; }
; __device__ __forceinline__ void attn_prep2(int bhA,int bhB,const float*logft,const float*nrm,__attribute__((address_space(3))) float*cumA,__attribute__((address_space(3))) float*cumB, ...
;     ...
;     const f4*p=(const f4*)(logft+(size_t)bh*SEQ)+2*tid; const f4 a=p[0],b=p[1];
;     w[x][0]=a.x; w[x][1]=w[x][0]+a.y; w[x][2]=w[x][1]+a.z; w[x][3]=w[x][2]+a.w; w[x][4]=w[x][3]+b.x; w[x][5]=w[x][4]+b.y; w[x][6]=w[x][5]+b.z; w[x][7]=w[x][6]+b.w;
;     incl[x]=w[x][7];
;     const int b_=bh/NHEAD,h_=bh%NHEAD; mq[x]=0.f; mk[x]=0.f;
;     const f4*q0p=(const f4*)(nrm+(size_t)(2*h_)*NR+(size_t)b_*SEQ)+2*tid,*q1p=(const f4*)(nrm+(size_t)(2*h_+1)*NR+(size_t)b_*SEQ)+2*tid;
;     const f4*k0p=(const f4*)(nrm+(size_t)(32+2*h_)*NR+(size_t)b_*SEQ)+2*tid,*k1p=(const f4*)(nrm+(size_t)(32+2*h_+1)*NR+(size_t)b_*SEQ)+2*tid;
; __device__ __forceinline__ void attn_phase(char*lds,const AttnTensors&T,const float*logft,const float*nrm,const float*b_f,__attribute__((address_space(3))) float*cumA,__attribute__((address_space(3))) float*cumB, ...
;     ...
;     { const int ln_=pg8::pg8_lane_id(),hh_=ln_&15; const float bv_=b_f[hh_]; int rk=0;
;       #pragma unroll
;       for(int g=0;g<NHEAD;++g){ const float bg=__builtin_bit_cast(float,__builtin_amdgcn_readlane(__builtin_bit_cast(int,bv_),g)); rk+=(bg<bv_||(bg==bv_&&g<hh_))?1:0; }
;       const unsigned long long mA_=__ballot(rk==p&&ln_<16),mB_=__ballot(rk==15-p&&ln_<16);
;       hA=__builtin_amdgcn_readfirstlane((int)__builtin_ctzll(mA_|(1ull<<63))&15); hB=__builtin_amdgcn_readfirstlane((int)__builtin_ctzll(mB_|(1ull<<63))&15); }
.LBB0_375:
	v_mbcnt_lo_u32_b32 v0, -1, 0
	v_mbcnt_hi_u32_b32 v0, -1, v0
	v_readlane_b32 s64, v254, 5
	v_and_b32_e32 v2, 15, v0
	v_lshlrev_b32_e32 v3, 2, v2
	v_readlane_b32 s65, v254, 6
	v_cmp_ne_u32_e64 s[10:11], 0, v2
	s_bfe_u32 s13, s58, 0x30003
	s_lshr_b32 s12, s58, 3
	v_readlane_b32 s75, v254, 16
	s_ashr_i32 s46, s58, 6
	global_load_dword v3, v3, s[64:65]
	v_mbcnt_lo_u32_b32 v23, -1, 0
	v_mbcnt_hi_u32_b32 v23, -1, v23
	v_readlane_b32 s76, v254, 17
	v_readlane_b32 s77, v254, 18
	v_readlane_b32 s78, v254, 19
	v_readlane_b32 s79, v254, 20
	v_readlane_b32 s66, v254, 7
	v_readlane_b32 s67, v254, 8
	v_readlane_b32 s68, v254, 9
	v_readlane_b32 s69, v254, 10
	v_readlane_b32 s70, v254, 11
	v_readlane_b32 s71, v254, 12
	v_readlane_b32 s72, v254, 13
	v_readlane_b32 s73, v254, 14
	v_readlane_b32 s74, v254, 15
	s_waitcnt vmcnt(0)
	v_readlane_b32 s8, v3, 0
	s_nop 1
	v_cmp_lt_f32_e32 vcc, s8, v3
	v_cmp_eq_f32_e64 s[8:9], s8, v3
	s_and_b64 s[8:9], s[10:11], s[8:9]
	s_or_b64 s[8:9], vcc, s[8:9]
	v_cndmask_b32_e64 v4, 0, 1, s[8:9]
	v_readlane_b32 s8, v3, 1
	v_cmp_lt_u32_e64 s[10:11], 1, v2
	s_nop 0
	v_cmp_lt_f32_e32 vcc, s8, v3
	v_cmp_eq_f32_e64 s[8:9], s8, v3
	s_and_b64 s[8:9], s[8:9], s[10:11]
	s_or_b64 vcc, vcc, s[8:9]
	v_addc_co_u32_e32 v4, vcc, 0, v4, vcc
	v_readlane_b32 s8, v3, 2
	v_cmp_lt_u32_e64 s[10:11], 2, v2
	s_nop 0
	v_cmp_lt_f32_e32 vcc, s8, v3
	v_cmp_eq_f32_e64 s[8:9], s8, v3
	s_and_b64 s[8:9], s[8:9], s[10:11]
	s_or_b64 s[8:9], vcc, s[8:9]
	v_cndmask_b32_e64 v5, 0, 1, s[8:9]
	v_readlane_b32 s8, v3, 3
	v_cmp_lt_u32_e64 s[10:11], 3, v2
	s_nop 0
	v_cmp_lt_f32_e32 vcc, s8, v3
	v_cmp_eq_f32_e64 s[8:9], s8, v3
	s_and_b64 s[8:9], s[8:9], s[10:11]
	s_or_b64 vcc, vcc, s[8:9]
	v_addc_co_u32_e32 v4, vcc, v4, v5, vcc
	v_readlane_b32 s8, v3, 4
	v_cmp_lt_u32_e64 s[10:11], 4, v2
	s_nop 0
	v_cmp_lt_f32_e32 vcc, s8, v3
	v_cmp_eq_f32_e64 s[8:9], s8, v3
	s_and_b64 s[8:9], s[8:9], s[10:11]
	s_or_b64 s[8:9], vcc, s[8:9]
	v_cndmask_b32_e64 v5, 0, 1, s[8:9]
	v_readlane_b32 s8, v3, 5
	v_cmp_lt_u32_e64 s[10:11], 5, v2
	s_nop 0
	v_cmp_lt_f32_e32 vcc, s8, v3
	v_cmp_eq_f32_e64 s[8:9], s8, v3
	s_and_b64 s[8:9], s[8:9], s[10:11]
	s_or_b64 vcc, vcc, s[8:9]
	v_addc_co_u32_e32 v4, vcc, v4, v5, vcc
	v_readlane_b32 s8, v3, 6
	v_cmp_lt_u32_e64 s[10:11], 6, v2
	s_nop 0
	v_cmp_lt_f32_e32 vcc, s8, v3
	v_cmp_eq_f32_e64 s[8:9], s8, v3
	s_and_b64 s[8:9], s[8:9], s[10:11]
	s_or_b64 s[8:9], vcc, s[8:9]
	v_cndmask_b32_e64 v5, 0, 1, s[8:9]
	v_readlane_b32 s8, v3, 7
	v_cmp_lt_u32_e64 s[10:11], 7, v2
	s_nop 0
	v_cmp_lt_f32_e32 vcc, s8, v3
	v_cmp_eq_f32_e64 s[8:9], s8, v3
	s_and_b64 s[8:9], s[8:9], s[10:11]
	s_or_b64 vcc, vcc, s[8:9]
	v_addc_co_u32_e32 v4, vcc, v4, v5, vcc
	v_readlane_b32 s8, v3, 8
	v_cmp_lt_u32_e64 s[10:11], 8, v2
	s_nop 0
	v_cmp_lt_f32_e32 vcc, s8, v3
	v_cmp_eq_f32_e64 s[8:9], s8, v3
	s_and_b64 s[8:9], s[8:9], s[10:11]
	s_or_b64 s[8:9], vcc, s[8:9]
	v_cndmask_b32_e64 v5, 0, 1, s[8:9]
	v_readlane_b32 s8, v3, 9
	v_cmp_lt_u32_e64 s[10:11], 9, v2
	s_nop 0
	v_cmp_lt_f32_e32 vcc, s8, v3
	v_cmp_eq_f32_e64 s[8:9], s8, v3
	s_and_b64 s[8:9], s[8:9], s[10:11]
	s_or_b64 vcc, vcc, s[8:9]
	v_addc_co_u32_e32 v4, vcc, v4, v5, vcc
	v_readlane_b32 s8, v3, 10
	v_cmp_lt_u32_e64 s[10:11], 10, v2
	s_nop 0
	v_cmp_lt_f32_e32 vcc, s8, v3
	v_cmp_eq_f32_e64 s[8:9], s8, v3
	s_and_b64 s[8:9], s[8:9], s[10:11]
	s_or_b64 s[8:9], vcc, s[8:9]
	v_cndmask_b32_e64 v5, 0, 1, s[8:9]
	v_readlane_b32 s8, v3, 11
	v_cmp_lt_u32_e64 s[10:11], 11, v2
	s_nop 0
	v_cmp_lt_f32_e32 vcc, s8, v3
	v_cmp_eq_f32_e64 s[8:9], s8, v3
	s_and_b64 s[8:9], s[8:9], s[10:11]
	s_or_b64 vcc, vcc, s[8:9]
	v_addc_co_u32_e32 v4, vcc, v4, v5, vcc
	v_readlane_b32 s8, v3, 12
	v_cmp_lt_u32_e64 s[10:11], 12, v2
	s_nop 0
	v_cmp_lt_f32_e32 vcc, s8, v3
	v_cmp_eq_f32_e64 s[8:9], s8, v3
	s_and_b64 s[8:9], s[8:9], s[10:11]
	s_or_b64 s[8:9], vcc, s[8:9]
	v_cndmask_b32_e64 v5, 0, 1, s[8:9]
	v_readlane_b32 s8, v3, 13
	v_cmp_lt_u32_e64 s[10:11], 13, v2
	s_nop 0
	v_cmp_lt_f32_e32 vcc, s8, v3
	v_cmp_eq_f32_e64 s[8:9], s8, v3
	s_and_b64 s[8:9], s[8:9], s[10:11]
	s_or_b64 vcc, vcc, s[8:9]
	v_addc_co_u32_e32 v4, vcc, v4, v5, vcc
	v_readlane_b32 s8, v3, 14
	v_cmp_eq_u32_e64 s[10:11], 15, v2
	s_nop 0
	v_cmp_lt_f32_e32 vcc, s8, v3
	v_cmp_eq_f32_e64 s[8:9], s8, v3
	s_and_b64 s[8:9], s[10:11], s[8:9]
	s_or_b64 vcc, vcc, s[8:9]
	v_readlane_b32 s8, v3, 15
	s_nop 1
	v_cmp_lt_f32_e64 s[8:9], s8, v3
	s_nop 1
	v_cndmask_b32_e64 v2, 0, 1, s[8:9]
	v_addc_co_u32_e32 v2, vcc, v4, v2, vcc
	v_cmp_eq_u32_e32 vcc, s13, v2
	v_cmp_gt_i32_e64 s[8:9], 16, v0
	s_and_b64 s[10:11], s[8:9], vcc
	v_cndmask_b32_e64 v0, 0, 1, s[10:11]
	v_cmp_ne_u32_e64 s[10:11], 0, v0
	v_bitop3_b32 v0, v2, s12, 7 bitop3:0x78
	v_cmp_eq_u32_e32 vcc, 15, v0
	s_and_b64 s[8:9], s[8:9], vcc
	v_cndmask_b32_e64 v0, 0, 1, s[8:9]
	v_cmp_ne_u32_e64 s[8:9], 0, v0
	s_bitset1_b32 s11, 31
	s_bitset1_b32 s9, 31
	s_ff1_i32_b64 s10, s[10:11]
	s_ff1_i32_b64 s8, s[8:9]
	v_readlane_b32 s9, v254, 2
	s_and_b32 s75, s10, 15
	s_and_b32 s64, s8, 15
	s_lshl_b32 s8, s46, 4
	v_add_u32_e32 v22, s9, v23
	s_or_b32 s10, s75, s8
	v_lshlrev_b32_e32 v2, 1, v22
	v_ashrrev_i32_e32 v3, 31, v2
	s_ashr_i32 s11, s10, 31
	v_lshlrev_b64 v[20:21], 4, v[2:3]
	s_lshr_b32 s9, s11, 28
	v_lshl_add_u64 v[18:19], s[86:87], 0, v[20:21]
	s_lshl_b64 s[12:13], s[10:11], 14
	s_add_i32 s9, s10, s9
	v_lshl_add_u64 v[2:3], v[18:19], 0, s[12:13]
	s_ashr_i32 s12, s9, 4
	s_and_b32 s9, s9, 0x7ffffff0
	s_sub_i32 s9, s10, s9
	s_lshl_b32 s10, s9, 1
	s_ashr_i32 s11, s10, 31
	s_or_b32 s8, s64, s8
	s_lshl_b64 s[14:15], s[10:11], 16
	s_add_u32 s9, s3, s14
	s_addc_u32 s11, s52, s15
	s_ashr_i32 s13, s12, 31
	s_lshl_b64 s[12:13], s[12:13], 14
	s_add_u32 s14, s9, s12
; __device__ __forceinline__ void attn_prep2(int bhA,int bhB,const float*logft,const float*nrm,__attribute__((address_space(3))) float*cumA,__attribute__((address_space(3))) float*cumB, ...
;     ...
;   for(int x=0;x<2;++x){ const int bh=x?bhB:bhA;
;     const f4*p=(const f4*)(logft+(size_t)bh*SEQ)+2*tid; const f4 a=p[0],b=p[1];
;     w[x][0]=a.x; w[x][1]=w[x][0]+a.y; w[x][2]=w[x][1]+a.z; w[x][3]=w[x][2]+a.w; w[x][4]=w[x][3]+b.x; w[x][5]=w[x][4]+b.y; w[x][6]=w[x][5]+b.z; w[x][7]=w[x][6]+b.w;
;     incl[x]=w[x][7];
;     const int b_=bh/NHEAD,h_=bh%NHEAD; mq[x]=0.f; mk[x]=0.f;
;     const f4*q0p=(const f4*)(nrm+(size_t)(2*h_)*NR+(size_t)b_*SEQ)+2*tid,*q1p=(const f4*)(nrm+(size_t)(2*h_+1)*NR+(size_t)b_*SEQ)+2*tid;
;     const f4*k0p=(const f4*)(nrm+(size_t)(32+2*h_)*NR+(size_t)b_*SEQ)+2*tid,*k1p=(const f4*)(nrm+(size_t)(32+2*h_+1)*NR+(size_t)b_*SEQ)+2*tid;
;     #pragma unroll
;     for(int j=0;j<2;++j){ const f4 qa=q0p[j]+q1p[j],ka=k0p[j]+k1p[j];
;       mq[x]=__builtin_fmaxf(mq[x],__builtin_fmaxf(__builtin_fmaxf(qa.x,qa.y),__builtin_fmaxf(qa.z,qa.w))); mk[x]=__builtin_fmaxf(mk[x],__builtin_fmaxf(__builtin_fmaxf(ka.x,ka.y),__builtin_fmaxf(ka.z,ka.w))); } }
	s_addc_u32 s15, s11, s13
	v_lshl_add_u64 v[14:15], s[14:15], 0, v[20:21]
	s_or_b32 s14, s10, 1
	s_ashr_i32 s15, s14, 31
	s_lshl_b64 s[14:15], s[14:15], 16
	s_add_u32 s9, s3, s14
	s_addc_u32 s11, s52, s15
	s_add_u32 s14, s9, s12
	s_addc_u32 s15, s11, s13
	v_lshl_add_u64 v[28:29], s[14:15], 0, v[20:21]
	s_lshl_b32 s98, s46, 4
	s_or_b32 s98, s98, s75
	s_lshl_b32 s99, s98, 14
	s_add_u32 s100, s86, s99
	s_addc_u32 s101, s87, 0
	v_lshl_add_u64 v[140:141], s[100:101], 0, v[20:21]
	global_load_dwordx4 v[60:63], v[140:141], off offset:16
	global_load_dwordx4 v[64:67], v[140:141], off
	s_and_b32 s99, s98, 15
	s_lshl_b32 s99, s99, 17
	s_ashr_i32 s100, s98, 4
	s_lshl_b32 s100, s100, 14
	s_add_u32 s99, s99, s100
	s_add_u32 s100, s3, s99
	s_addc_u32 s101, s52, 0
	v_lshl_add_u64 v[142:143], s[100:101], 0, v[20:21]
	global_load_dwordx4 v[68:71], v[142:143], off offset:16
	global_load_dwordx4 v[72:75], v[142:143], off
	s_add_u32 s100, s100, 0x10000
	s_addc_u32 s101, s101, 0
	v_lshl_add_u64 v[144:145], s[100:101], 0, v[20:21]
	global_load_dwordx4 v[76:79], v[144:145], off offset:16
	global_load_dwordx4 v[80:83], v[144:145], off
	s_add_u32 s100, s100, 0x1f0000
	s_addc_u32 s101, s101, 0
	v_lshl_add_u64 v[146:147], s[100:101], 0, v[20:21]
	global_load_dwordx4 v[84:87], v[146:147], off offset:16
	global_load_dwordx4 v[88:91], v[146:147], off
	s_add_u32 s100, s100, 0x10000
	s_addc_u32 s101, s101, 0
	v_lshl_add_u64 v[148:149], s[100:101], 0, v[20:21]
	global_load_dwordx4 v[92:95], v[148:149], off offset:16
	global_load_dwordx4 v[96:99], v[148:149], off
	s_lshl_b32 s98, s46, 4
	s_or_b32 s98, s98, s64
	s_lshl_b32 s99, s98, 14
	s_add_u32 s100, s86, s99
	s_addc_u32 s101, s87, 0
	v_lshl_add_u64 v[150:151], s[100:101], 0, v[20:21]
	global_load_dwordx4 v[100:103], v[150:151], off offset:16
	global_load_dwordx4 v[104:107], v[150:151], off
	s_and_b32 s99, s98, 15
	s_lshl_b32 s99, s99, 17
	s_ashr_i32 s100, s98, 4
	s_lshl_b32 s100, s100, 14
	s_add_u32 s99, s99, s100
	s_add_u32 s100, s3, s99
	s_addc_u32 s101, s52, 0
	v_lshl_add_u64 v[152:153], s[100:101], 0, v[20:21]
	global_load_dwordx4 v[108:111], v[152:153], off offset:16
	global_load_dwordx4 v[112:115], v[152:153], off
	s_add_u32 s100, s100, 0x10000
	s_addc_u32 s101, s101, 0
	v_lshl_add_u64 v[154:155], s[100:101], 0, v[20:21]
	global_load_dwordx4 v[116:119], v[154:155], off offset:16
	global_load_dwordx4 v[120:123], v[154:155], off
	s_add_u32 s100, s100, 0x1f0000
	s_addc_u32 s101, s101, 0
	v_lshl_add_u64 v[156:157], s[100:101], 0, v[20:21]
	global_load_dwordx4 v[124:127], v[156:157], off offset:16
	global_load_dwordx4 v[128:131], v[156:157], off
	s_add_u32 s100, s100, 0x10000
	s_addc_u32 s101, s101, 0
	v_lshl_add_u64 v[158:159], s[100:101], 0, v[20:21]
	global_load_dwordx4 v[132:135], v[158:159], off offset:16
	global_load_dwordx4 v[136:139], v[158:159], off
	global_load_dwordx4 v[10:13], v[2:3], off offset:16
	global_load_dwordx4 v[6:9], v[2:3], off
	s_nop 0
	global_load_dwordx4 v[2:5], v[14:15], off offset:16
	s_nop 0
	global_load_dwordx4 v[14:17], v[14:15], off
	s_nop 0
	global_load_dwordx4 v[24:27], v[28:29], off offset:16
	s_nop 0
	global_load_dwordx4 v[28:31], v[28:29], off
	s_add_i32 s14, s10, 32
	s_mov_b32 s15, s91
	s_lshl_b64 s[14:15], s[14:15], 16
	s_add_u32 s9, s3, s14
	s_addc_u32 s11, s52, s15
	s_add_u32 s14, s9, s12
	s_addc_u32 s15, s11, s13
	s_add_i32 s10, s10, 33
	s_mov_b32 s11, s91
	s_lshl_b64 s[10:11], s[10:11], 16
	s_add_u32 s9, s3, s10
	s_addc_u32 s11, s52, s11
	s_add_u32 s10, s9, s12
	s_addc_u32 s11, s11, s13
	v_lshl_add_u64 v[32:33], s[14:15], 0, v[20:21]
	v_lshl_add_u64 v[36:37], s[10:11], 0, v[20:21]
	s_ashr_i32 s9, s8, 31
	s_lshl_b64 s[10:11], s[8:9], 14
	s_lshr_b32 s9, s9, 28
	s_add_i32 s9, s8, s9
	v_cmp_gt_i32_e32 vcc, 1, v23
	s_waitcnt vmcnt(1)
	v_pk_add_f32 v[4:5], v[4:5], v[26:27]
	s_waitcnt vmcnt(0)
	v_pk_add_f32 v[40:41], v[16:17], v[30:31]
	v_pk_add_f32 v[42:43], v[14:15], v[28:29]
	global_load_dwordx4 v[14:17], v[32:33], off offset:16
	global_load_dwordx4 v[28:31], v[32:33], off
	s_nop 0
	global_load_dwordx4 v[32:35], v[36:37], off offset:16
	s_nop 0
	global_load_dwordx4 v[36:39], v[36:37], off
	v_max_f32_e32 v0, v40, v41
	v_pk_add_f32 v[2:3], v[2:3], v[24:25]
	v_max_f32_e32 v4, v4, v5
	v_max3_f32 v0, v42, v43, v0
	v_max3_f32 v2, v2, v3, v4
	v_max3_f32 v24, v0, 0, v2
	v_lshl_add_u64 v[2:3], v[18:19], 0, s[10:11]
	s_ashr_i32 s10, s9, 4
	s_and_b32 s9, s9, 0x7ffffff0
	s_sub_i32 s8, s8, s9
	s_lshl_b32 s8, s8, 1
	s_ashr_i32 s9, s8, 31
	s_lshl_b64 s[12:13], s[8:9], 16
	s_add_u32 s9, s3, s12
	s_addc_u32 s13, s52, s13
	s_ashr_i32 s11, s10, 31
	s_lshl_b64 s[10:11], s[10:11], 14
	s_add_u32 s12, s9, s10
	s_addc_u32 s13, s13, s11
	s_waitcnt vmcnt(1)
	v_pk_add_f32 v[16:17], v[16:17], v[34:35]
	s_waitcnt vmcnt(0)
	v_pk_add_f32 v[30:31], v[30:31], v[38:39]
	v_pk_add_f32 v[28:29], v[28:29], v[36:37]
	v_max_f32_e32 v30, v30, v31
	v_pk_add_f32 v[14:15], v[14:15], v[32:33]
	v_max_f32_e32 v0, v16, v17
	v_max3_f32 v28, v28, v29, v30
	v_max3_f32 v0, v14, v15, v0
	v_max3_f32 v0, v28, 0, v0
	global_load_dwordx4 v[26:29], v[2:3], off offset:16
	s_nop 0
	global_load_dwordx4 v[2:5], v[2:3], off
	v_lshl_add_u64 v[30:31], s[12:13], 0, v[20:21]
	s_or_b32 s12, s8, 1
	v_mov_b32_e32 v14, v6
	v_mov_b32_e32 v16, v7
	s_ashr_i32 s13, s12, 31
	s_lshl_b64 s[12:13], s[12:13], 16
	s_add_u32 s9, s3, s12
	s_addc_u32 s13, s52, s13
	s_add_u32 s12, s9, s10
	s_addc_u32 s13, s13, s11
	v_lshl_add_u64 v[38:39], s[12:13], 0, v[20:21]
	s_add_i32 s12, s8, 32
	s_mov_b32 s13, s91
	s_lshl_b64 s[12:13], s[12:13], 16
	s_add_u32 s9, s3, s12
	s_addc_u32 s13, s52, s13
	s_add_u32 s12, s9, s10
	s_addc_u32 s13, s13, s11
	s_add_i32 s8, s8, 33
	s_mov_b32 s9, s91
	s_lshl_b64 s[8:9], s[8:9], 16
	s_add_u32 s8, s3, s8
	s_addc_u32 s9, s52, s9
	s_add_u32 s8, s8, s10
	v_lshl_add_u64 v[42:43], s[12:13], 0, v[20:21]
	s_addc_u32 s9, s9, s11
	v_lshl_add_u64 v[20:21], s[8:9], 0, v[20:21]
	s_mov_b64 s[8:9], 0
	s_waitcnt vmcnt(0)
; __device__ __forceinline__ void attn_prep2(int bhA,int bhB,const float*logft,const float*nrm,__attribute__((address_space(3))) float*cumA,__attribute__((address_space(3))) float*cumB, ...
;     ...
;     w[x][0]=a.x; w[x][1]=w[x][0]+a.y; w[x][2]=w[x][1]+a.z; w[x][3]=w[x][2]+a.w; w[x][4]=w[x][3]+b.x; w[x][5]=w[x][4]+b.y; w[x][6]=w[x][5]+b.z; w[x][7]=w[x][6]+b.w;
;     incl[x]=w[x][7];
;     const int b_=bh/NHEAD,h_=bh%NHEAD; mq[x]=0.f; mk[x]=0.f;
;     const f4*q0p=(const f4*)(nrm+(size_t)(2*h_)*NR+(size_t)b_*SEQ)+2*tid,*q1p=(const f4*)(nrm+(size_t)(2*h_+1)*NR+(size_t)b_*SEQ)+2*tid;
;     const f4*k0p=(const f4*)(nrm+(size_t)(32+2*h_)*NR+(size_t)b_*SEQ)+2*tid,*k1p=(const f4*)(nrm+(size_t)(32+2*h_+1)*NR+(size_t)b_*SEQ)+2*tid;
;     #pragma unroll
;     for(int j=0;j<2;++j){ const f4 qa=q0p[j]+q1p[j],ka=k0p[j]+k1p[j];
;       mq[x]=__builtin_fmaxf(mq[x],__builtin_fmaxf(__builtin_fmaxf(qa.x,qa.y),__builtin_fmaxf(qa.z,qa.w))); mk[x]=__builtin_fmaxf(mk[x],__builtin_fmaxf(__builtin_fmaxf(ka.x,ka.y),__builtin_fmaxf(ka.z,ka.w))); } }
;   #pragma unroll
;   for(int o=1;o<64;o<<=1){
;     #pragma unroll
;     for(int x=0;x<2;++x){ const float t_=__builtin_bit_cast(float,__builtin_amdgcn_ds_bpermute((lane-o)*4,__builtin_bit_cast(int,incl[x]))); if(lane>=o)incl[x]+=t_;
;       mq[x]=__builtin_fmaxf(mq[x],__builtin_bit_cast(float,__builtin_amdgcn_ds_bpermute((lane^o)*4,__builtin_bit_cast(int,mq[x])))); mk[x]=__builtin_fmaxf(mk[x],__builtin_bit_cast(float,__builtin_amdgcn_ds_bpermute((lane^o)*4,__builtin_bit_cast(int,mk[x])))); } }
	v_mov_b32_e32 v15, v2
	v_mov_b32_e32 v17, v3
	v_pk_add_f32 v[18:19], v[14:15], v[16:17]
	v_mov_b32_e32 v14, v8
	v_mov_b32_e32 v15, v4
	v_pk_add_f32 v[14:15], v[14:15], v[18:19]
	v_mov_b32_e32 v4, v9
	v_pk_add_f32 v[16:17], v[4:5], v[14:15]
	v_mov_b32_e32 v4, v10
	v_mov_b32_e32 v5, v26
	v_pk_add_f32 v[4:5], v[4:5], v[16:17]
	v_mov_b32_e32 v26, v11
	v_pk_add_f32 v[8:9], v[26:27], v[4:5]
	v_mov_b32_e32 v10, v12
	v_mov_b32_e32 v11, v28
	v_pk_add_f32 v[10:11], v[10:11], v[8:9]
	v_mov_b32_e32 v28, v13
	v_pk_add_f32 v[12:13], v[28:29], v[10:11]
	global_load_dwordx4 v[26:29], v[30:31], off offset:16
	s_nop 0
	global_load_dwordx4 v[30:33], v[30:31], off
	s_nop 0
	global_load_dwordx4 v[34:37], v[38:39], off offset:16
	s_nop 0
	global_load_dwordx4 v[38:41], v[38:39], off
	s_waitcnt vmcnt(1)
	v_pk_add_f32 v[26:27], v[26:27], v[34:35]
	s_waitcnt vmcnt(0)
	v_pk_add_f32 v[50:51], v[32:33], v[40:41]
	v_pk_add_f32 v[52:53], v[30:31], v[38:39]
	global_load_dwordx4 v[30:33], v[42:43], off offset:16
	global_load_dwordx4 v[38:41], v[42:43], off
	s_nop 0
	global_load_dwordx4 v[42:45], v[20:21], off offset:16
	global_load_dwordx4 v[46:49], v[20:21], off
	v_max_f32_e32 v3, v50, v51
	v_max3_f32 v3, v52, v53, v3
	s_waitcnt vmcnt(1)
	v_pk_add_f32 v[30:31], v[30:31], v[42:43]
	s_waitcnt vmcnt(0)
	v_pk_add_f32 v[20:21], v[40:41], v[48:49]
	v_pk_add_f32 v[38:39], v[38:39], v[46:47]
	v_max_f32_e32 v7, v20, v21
	v_pk_add_f32 v[20:21], v[28:29], v[36:37]
	v_pk_add_f32 v[28:29], v[32:33], v[44:45]
	v_max_f32_e32 v20, v20, v21
	v_max3_f32 v20, v26, v27, v20
	v_max3_f32 v3, v3, 0, v20
	v_max_f32_e32 v20, v28, v29
	v_max3_f32 v7, v38, v39, v7
	v_max3_f32 v20, v30, v31, v20
	v_max3_f32 v20, v7, 0, v20
	v_lshlrev_b32_e32 v7, 2, v23
	v_xor_b32_e32 v25, 4, v7
	ds_bpermute_b32 v27, v25, v24
	v_add_u32_e32 v21, -4, v7
	ds_bpermute_b32 v26, v21, v12
	ds_bpermute_b32 v21, v21, v13
	v_xor_b32_e32 v30, 0x80, v7
	s_waitcnt lgkmcnt(2)
	v_max_f32_e32 v27, v27, v27
	v_max_f32_e32 v24, v24, v27
	ds_bpermute_b32 v27, v25, v0
	s_waitcnt lgkmcnt(2)
	v_add_f32_e32 v26, v12, v26
	s_waitcnt lgkmcnt(1)
	v_add_f32_e32 v21, v13, v21
	v_cndmask_b32_e32 v21, v21, v13, vcc
	v_cndmask_b32_e32 v26, v26, v12, vcc
	s_waitcnt lgkmcnt(0)
	v_max_f32_e32 v27, v27, v27
	v_max_f32_e32 v0, v0, v27
	ds_bpermute_b32 v27, v25, v3
	ds_bpermute_b32 v25, v25, v20
	v_cmp_gt_i32_e32 vcc, 2, v23
	s_waitcnt lgkmcnt(1)
	v_max_f32_e32 v27, v27, v27
	s_waitcnt lgkmcnt(0)
	v_max_f32_e32 v25, v25, v25
	v_max_f32_e32 v20, v20, v25
	v_add_u32_e32 v25, -8, v7
	ds_bpermute_b32 v28, v25, v26
	ds_bpermute_b32 v25, v25, v21
	v_max_f32_e32 v3, v3, v27
	v_xor_b32_e32 v27, 8, v7
	ds_bpermute_b32 v29, v27, v24
	s_waitcnt lgkmcnt(2)
	v_add_f32_e32 v28, v26, v28
	s_waitcnt lgkmcnt(1)
	v_add_f32_e32 v25, v21, v25
	v_cndmask_b32_e32 v21, v25, v21, vcc
	v_cndmask_b32_e32 v25, v28, v26, vcc
	ds_bpermute_b32 v26, v27, v3
	s_waitcnt lgkmcnt(1)
	v_max_f32_e32 v29, v29, v29
	v_max_f32_e32 v24, v24, v29
	ds_bpermute_b32 v29, v27, v0
	v_cmp_gt_i32_e32 vcc, 4, v23
	s_waitcnt lgkmcnt(1)
	v_max_f32_e32 v26, v26, v26
	v_max_f32_e32 v3, v3, v26
	ds_bpermute_b32 v26, v27, v20
	v_xor_b32_e32 v27, 16, v7
	s_waitcnt lgkmcnt(1)
	v_max_f32_e32 v29, v29, v29
	v_max_f32_e32 v0, v0, v29
	ds_bpermute_b32 v29, v27, v24
	s_waitcnt lgkmcnt(1)
	v_max_f32_e32 v26, v26, v26
	v_max_f32_e32 v20, v20, v26
	v_add_u32_e32 v26, -16, v7
	ds_bpermute_b32 v28, v26, v25
	ds_bpermute_b32 v26, v26, v21
	s_waitcnt lgkmcnt(2)
	v_max_f32_e32 v29, v29, v29
	v_max_f32_e32 v24, v24, v29
	ds_bpermute_b32 v29, v27, v0
	s_waitcnt lgkmcnt(2)
	v_add_f32_e32 v28, v25, v28
	s_waitcnt lgkmcnt(1)
	v_add_f32_e32 v26, v21, v26
	v_cndmask_b32_e32 v21, v26, v21, vcc
	ds_bpermute_b32 v26, v27, v3
	v_cndmask_b32_e32 v25, v28, v25, vcc
	v_cmp_gt_i32_e32 vcc, 8, v23
	s_waitcnt lgkmcnt(1)
	v_max_f32_e32 v29, v29, v29
	v_max_f32_e32 v0, v0, v29
	s_waitcnt lgkmcnt(0)
	v_max_f32_e32 v26, v26, v26
	v_max_f32_e32 v3, v3, v26
	ds_bpermute_b32 v26, v27, v20
	v_xor_b32_e32 v27, 32, v7
	ds_bpermute_b32 v29, v27, v24
	s_waitcnt lgkmcnt(1)
	v_max_f32_e32 v26, v26, v26
	v_max_f32_e32 v20, v20, v26
	v_subrev_u32_e32 v26, 32, v7
	ds_bpermute_b32 v28, v26, v25
	ds_bpermute_b32 v26, v26, v21
	s_waitcnt lgkmcnt(2)
	v_max_f32_e32 v29, v29, v29
	v_max_f32_e32 v24, v24, v29
	ds_bpermute_b32 v29, v27, v0
	s_waitcnt lgkmcnt(2)
	v_add_f32_e32 v28, v25, v28
	s_waitcnt lgkmcnt(1)
	v_add_f32_e32 v26, v21, v26
	v_cndmask_b32_e32 v21, v26, v21, vcc
	v_cndmask_b32_e32 v26, v28, v25, vcc
	ds_bpermute_b32 v25, v27, v3
	s_waitcnt lgkmcnt(1)
	v_max_f32_e32 v29, v29, v29
	v_max_f32_e32 v0, v0, v29
	v_cmp_gt_i32_e32 vcc, 16, v23
	s_waitcnt lgkmcnt(0)
	v_max_f32_e32 v25, v25, v25
	v_max_f32_e32 v28, v3, v25
	ds_bpermute_b32 v3, v27, v20
	v_xor_b32_e32 v27, 64, v7
	s_waitcnt lgkmcnt(0)
	v_max_f32_e32 v3, v3, v3
	v_max_f32_e32 v20, v20, v3
	v_subrev_u32_e32 v3, 64, v7
	ds_bpermute_b32 v25, v3, v26
	s_waitcnt lgkmcnt(0)
	v_add_f32_e32 v29, v26, v25
	ds_bpermute_b32 v25, v27, v24
	s_waitcnt lgkmcnt(0)
	v_max_f32_e32 v25, v25, v25
	v_max_f32_e32 v24, v24, v25
	ds_bpermute_b32 v25, v27, v0
	s_waitcnt lgkmcnt(0)
	v_max_f32_e32 v25, v25, v25
	v_max_f32_e32 v25, v0, v25
	ds_bpermute_b32 v0, v3, v21
	s_waitcnt lgkmcnt(0)
	v_add_f32_e32 v0, v21, v0
	v_cndmask_b32_e32 v3, v0, v21, vcc
	ds_bpermute_b32 v21, v27, v28
	v_cndmask_b32_e32 v0, v29, v26, vcc
	v_cmp_gt_i32_e32 vcc, 32, v23
	s_waitcnt lgkmcnt(0)
	v_max_f32_e32 v21, v21, v21
	v_max_f32_e32 v26, v28, v21
	ds_bpermute_b32 v21, v27, v20
	ds_bpermute_b32 v28, v30, v25
	ds_bpermute_b32 v29, v30, v26
	s_waitcnt lgkmcnt(2)
	v_max_f32_e32 v21, v21, v21
	v_max_f32_e32 v27, v20, v21
	v_add_u32_e32 v21, 0xffffff80, v7
	ds_bpermute_b32 v7, v21, v0
	ds_bpermute_b32 v21, v21, v3
	s_waitcnt lgkmcnt(1)
	v_add_f32_e32 v7, v0, v7
	v_cndmask_b32_e32 v20, v7, v0, vcc
	ds_bpermute_b32 v7, v30, v24
	ds_bpermute_b32 v30, v30, v27
	s_waitcnt lgkmcnt(2)
	v_add_f32_e32 v21, v3, v21
	v_cndmask_b32_e32 v21, v21, v3, vcc
	v_cndmask_b32_e32 v20, v20, v0, vcc
	v_cmp_lt_i32_e32 vcc, 62, v23
	s_and_saveexec_b64 s[10:11], vcc
	v_readlane_b32 s76, v254, 57
	s_xor_b64 s[10:11], exec, s[10:11]
	v_readlane_b32 s77, v254, 58
	v_readlane_b32 s78, v254, 59
	v_readlane_b32 s79, v254, 60
	v_readlane_b32 s80, v254, 61
	v_readlane_b32 s81, v254, 62
	v_readlane_b32 s82, v254, 63
	v_readlane_b32 s83, v255, 0
	s_cbranch_execnz .LBB0_534
	s_or_saveexec_b64 s[10:11], s[10:11]
	v_mov_b32_e32 v3, s85
	s_xor_b64 exec, exec, s[10:11]
	s_cbranch_execnz .LBB0_537
